# baseline (speedup 1.0000x reference)
.LBB1_52:
	s_or_b64 exec, exec, s[8:9]
	v_lshlrev_b32_e32 v1, 1, v0
	s_movk_i32 s8, 0xc4
	v_cmp_gt_u32_e64 s[10:11], s8, v0
	v_mov_b32_e32 v53, 0
	v_lshlrev_b32_e32 v56, 2, v1
	v_mov_b32_e32 v55, 0
	s_waitcnt lgkmcnt(0)
	s_barrier
	s_and_saveexec_b64 s[8:9], s[10:11]
	ds_read_b32 v55, v56 offset:4160
	s_or_b64 exec, exec, s[8:9]
	v_or_b32_e32 v54, 1, v1
	s_movk_i32 s8, 0x187
	v_cmp_gt_u32_e64 s[8:9], s8, v54
	s_and_saveexec_b64 s[12:13], s[8:9]
	ds_read_b32 v53, v56 offset:4164
	s_or_b64 exec, exec, s[12:13]
	s_waitcnt lgkmcnt(0)
	v_add_u32_e32 v56, v53, v55
	v_mov_b32_e32 v60, v55
	v_mov_b32_e32 v61, v53
	v_lshlrev_b32_e32 v64, 8, v0
	s_and_saveexec_b64 s[12:13], s[10:11]
	global_atomic_add_x2 v[62:63], v64, v[60:61], s[16:17] sc0
	s_mov_b64 exec, s[12:13]
	v_mov_b32_e32 v57, v56
	v_lshrrev_b32_e32 v59, 6, v0
	v_and_b32_e32 v58, 63, v0
	v_add_u32_dpp v57, v57, v57 row_shr:1 row_mask:0xf bank_mask:0xf bound_ctrl:1
	s_nop 1
	v_add_u32_dpp v57, v57, v57 row_shr:2 row_mask:0xf bank_mask:0xf bound_ctrl:1
	s_nop 1
	v_add_u32_dpp v57, v57, v57 row_shr:4 row_mask:0xf bank_mask:0xf bound_ctrl:1
	s_nop 1
	v_add_u32_dpp v57, v57, v57 row_shr:8 row_mask:0xf bank_mask:0xf bound_ctrl:1
	s_nop 1
	v_add_u32_dpp v57, v57, v57 row_bcast:15 row_mask:0xa bank_mask:0xf
	s_nop 1
	v_add_u32_dpp v57, v57, v57 row_bcast:31 row_mask:0xc bank_mask:0xf
	v_cmp_eq_u32_e64 s[12:13], 63, v58
	v_lshlrev_b32_e32 v58, 2, v59
	s_and_saveexec_b64 s[14:15], s[12:13]
	ds_write_b32 v58, v57
	s_mov_b64 exec, s[14:15]
	s_waitcnt lgkmcnt(0)
	s_barrier
	v_mov_b32_e32 v58, 0
	ds_read_b128 v[66:69], v58
	v_cmp_lt_u32_e64 s[42:43], 0, v59
	v_cmp_lt_u32_e64 s[12:13], 1, v59
	v_cmp_lt_u32_e64 s[14:15], 2, v59
	s_waitcnt lgkmcnt(0)
	v_cndmask_b32_e64 v66, 0, v66, s[42:43]
	v_cndmask_b32_e64 v67, 0, v67, s[12:13]
	v_cndmask_b32_e64 v68, 0, v68, s[14:15]
	v_add3_u32 v57, v57, v66, v67
	v_add_u32_e32 v57, v57, v68
	v_add_u32_e32 v40, v40, v34
	v_sub_u32_e32 v56, v57, v56
	s_and_saveexec_b64 s[12:13], s[10:11]
	s_cbranch_execz .LBB1_80
	ds_write_b32 v40, v56 offset:1024
	v_add_u32_e32 v58, v56, v55
	s_and_saveexec_b64 s[14:15], s[8:9]
	ds_write_b32 v40, v58 offset:1028
